# speedup vs baseline: 1.1232x; 1.0036x over previous
.LBB0_7:
	s_or_b64 exec, exec, s[4:5]
	s_mov_b32 s34, 0xe52632a
	v_writelane_b32 v20, s34, 0
	s_mov_b32 s34, 0x2102e45
	v_writelane_b32 v20, s34, 1
	s_mov_b32 s34, 0x1f202f6f
	v_writelane_b32 v20, s34, 2
	s_mov_b32 s34, 0x142d0a56
	v_writelane_b32 v20, s34, 3
	s_mov_b32 s34, 0x2b1c1160
	v_writelane_b32 v20, s34, 4
	s_mov_b32 s34, 0x47394854
	v_writelane_b32 v20, s34, 5
	s_mov_b32 s34, 0x12071303
	v_writelane_b32 v20, s34, 6
	s_mov_b32 s34, 0x15746465
	v_writelane_b32 v20, s34, 7
	s_mov_b32 s34, 0x2b5a3e22
	v_writelane_b32 v20, s34, 8
	s_mov_b32 s34, 0x34176831
	v_writelane_b32 v20, s34, 9
	s_mov_b32 s34, 0x50354d33
	v_writelane_b32 v20, s34, 10
	s_mov_b32 s34, 0x1b43114f
	v_writelane_b32 v20, s34, 11
	s_mov_b32 s34, 0x3d66413c
	v_writelane_b32 v20, s34, 12
	s_mov_b32 s34, 0x9235c30
	v_writelane_b32 v20, s34, 13
	s_mov_b32 s34, 0x40695d59
	v_writelane_b32 v20, s34, 14
	s_mov_b32 s34, 0x5e361a4e
	v_writelane_b32 v20, s34, 15
	s_mov_b32 s34, 0x1441d
	v_writelane_b32 v20, s34, 16
	s_mov_b32 s34, 0x46625370
	v_writelane_b32 v20, s34, 17
	s_mov_b32 s34, 0x572c1e3b
	v_writelane_b32 v20, s34, 18
	s_mov_b32 s34, 0x72054b4a
	v_writelane_b32 v20, s34, 19
	s_mov_b32 s34, 0xf37616e
	v_writelane_b32 v20, s34, 20
	s_mov_b32 s34, 0x4376171
	v_writelane_b32 v20, s34, 21
	s_mov_b32 s34, 0x49373821
	v_writelane_b32 v20, s34, 22
	s_mov_b32 s34, 0x4c735516
	v_writelane_b32 v20, s34, 23
	s_mov_b32 s34, 0x25763a77
	v_writelane_b32 v20, s34, 24
	s_mov_b32 s34, 0x266a5827
	v_writelane_b32 v20, s34, 25
	s_mov_b32 s34, 0x190b676c
	v_writelane_b32 v20, s34, 26
	s_mov_b32 s34, 0xd51296d
	v_writelane_b32 v20, s34, 27
	s_mov_b32 s34, 0x8067524
	v_writelane_b32 v20, s34, 28
	s_mov_b32 s34, 0x323f4418
	v_writelane_b32 v20, s34, 29
	s_mov_b32 s34, 0x5b780c42
	v_writelane_b32 v20, s34, 30
	s_mov_b32 s34, 0x6b285f1d
	v_writelane_b32 v20, s34, 31
	s_mov_b32 s34, 0x38587000
	v_writelane_b32 v22, s34, 0
	s_mov_b32 s34, 0xa878
	v_writelane_b32 v23, s34, 0
	s_mov_b32 s34, 0x80482830
	v_writelane_b32 v22, s34, 1
	s_mov_b32 s34, 0xa068
	v_writelane_b32 v23, s34, 1
	s_mov_b32 s34, 0x59790191
	v_writelane_b32 v22, s34, 2
	s_mov_b32 s34, 0x3971
	v_writelane_b32 v23, s34, 2
	s_mov_b32 s34, 0x9949515a
	v_writelane_b32 v22, s34, 3
	s_mov_b32 s34, 0x2969
	v_writelane_b32 v23, s34, 3
	s_mov_b32 s34, 0x222422a
	v_writelane_b32 v22, s34, 4
	s_mov_b32 s34, 0x3a72
	v_writelane_b32 v23, s34, 4
	s_mov_b32 s34, 0x329a1a03
	v_writelane_b32 v22, s34, 5
	s_mov_b32 s34, 0x8a6a
	v_writelane_b32 v23, s34, 5
	s_mov_b32 s34, 0x5b23934b
	v_writelane_b32 v22, s34, 6
	s_mov_b32 s34, 0x3b73
	v_writelane_b32 v23, s34, 6
	s_mov_b32 s34, 0x83541374
	v_writelane_b32 v22, s34, 7
	s_mov_b32 s34, 0x336b
	v_writelane_b32 v23, s34, 7
	s_mov_b32 s34, 0x3c1c2434
	v_writelane_b32 v22, s34, 8
	s_mov_b32 s34, 0x48c
	v_writelane_b32 v23, s34, 8
	s_mov_b32 s34, 0x4c1da455
	v_writelane_b32 v22, s34, 9
	s_mov_b32 s34, 0x449c
	v_writelane_b32 v23, s34, 9
	s_mov_b32 s34, 0x8d25052d
	v_writelane_b32 v22, s34, 10
	s_mov_b32 s34, 0x9d5d
	v_writelane_b32 v23, s34, 10
	s_mov_b32 s34, 0x761e4556
	v_writelane_b32 v22, s34, 11
	s_mov_b32 s34, 0x3565
	v_writelane_b32 v23, s34, 11
	s_mov_b32 s34, 0x46368e6e
	v_writelane_b32 v22, s34, 12
	s_mov_b32 s34, 0x63e
	v_writelane_b32 v23, s34, 12
	s_mov_b32 s34, 0x5f579e77
	v_writelane_b32 v22, s34, 13
	s_mov_b32 s34, 0x2ea6
	v_writelane_b32 v23, s34, 13
	s_mov_b32 s34, 0x174f1f9f
	v_writelane_b32 v22, s34, 14
	s_mov_b32 s34, 0x278f
	v_writelane_b32 v23, s34, 14
	s_mov_b32 s34, 0x38584700
	v_writelane_b32 v22, s34, 15
	s_mov_b32 s34, 0xa897
	v_writelane_b32 v23, s34, 15
	s_mov_b32 s34, 0x90982008
	v_writelane_b32 v22, s34, 16
	s_mov_b32 s34, 0x4060
	v_writelane_b32 v23, s34, 16
	s_mov_b32 s34, 0x411810a1
	v_writelane_b32 v22, s34, 17
	s_mov_b32 s34, 0x5088
	v_writelane_b32 v23, s34, 17
	s_mov_b32 s34, 0x8161197a
	v_writelane_b32 v22, s34, 18
	s_mov_b32 s34, 0x2109
	v_writelane_b32 v23, s34, 18
	s_mov_b32 s34, 0x12314aa2
	v_writelane_b32 v22, s34, 19
	s_mov_b32 s34, 0x1189
	v_writelane_b32 v23, s34, 19
	s_mov_b32 s34, 0x520a430b
	v_writelane_b32 v22, s34, 20
	s_mov_b32 s34, 0x6292
	v_writelane_b32 v23, s34, 20
	s_mov_b32 s34, 0x9b828b53
	v_writelane_b32 v22, s34, 21
	s_mov_b32 s34, 0x2b63
	v_writelane_b32 v23, s34, 21
	s_mov_b32 s34, 0x7c7b5c84
	v_writelane_b32 v22, s34, 22
	s_mov_b32 s34, 0xa31b
	v_writelane_b32 v23, s34, 22
	s_mov_b32 s34, 0x6c0c957d
	v_writelane_b32 v22, s34, 23
	s_mov_b32 s34, 0x942c
	v_writelane_b32 v23, s34, 23
	s_mov_b32 s34, 0x753d85a5
	v_writelane_b32 v22, s34, 24
	s_mov_b32 s34, 0x6414
	v_writelane_b32 v23, s34, 24
	s_mov_b32 s34, 0x5e6d7e26
	v_writelane_b32 v22, s34, 25
	s_mov_b32 s34, 0x4d0d
	v_writelane_b32 v23, s34, 25
	s_mov_b32 s34, 0x8666160f
	v_writelane_b32 v22, s34, 26
	s_mov_b32 s34, 0x9615
	v_writelane_b32 v23, s34, 26
	s_mov_b32 s34, 0x2f7f0787
	v_writelane_b32 v22, s34, 27
	s_mov_b32 s34, 0x4e0e
	v_writelane_b32 v23, s34, 27
	s_mov_b32 s34, 0xa76f2008
	v_writelane_b32 v22, s34, 28
	s_mov_b32 s34, 0x373f
	v_writelane_b32 v23, s34, 28
	s_mov_b32 s34, 0x90982008
	v_writelane_b32 v22, s34, 29
	s_mov_b32 s34, 0x4067
	v_writelane_b32 v23, s34, 29
	s_mov_b32 s34, 0x90982008
	v_writelane_b32 v22, s34, 30
	s_mov_b32 s34, 0x4060
	v_writelane_b32 v23, s34, 30
	s_mov_b32 s34, 0x90982008
	v_writelane_b32 v22, s34, 31
	s_mov_b32 s34, 0x4060
	v_writelane_b32 v23, s34, 31
	s_add_u32 s32, s20, s30
	s_addc_u32 s33, s21, 0
	v_lshlrev_b32_e32 v21, 2, v0
	v_add_u32_e32 v21, 0x21000, v21
	v_cmp_gt_u32_e32 vcc, 32, v0
	s_and_saveexec_b64 s[4:5], vcc
	global_store_dword v21, v20, s[32:33]
	global_store_dword v21, v22, s[32:33] offset:128
	global_store_dword v21, v23, s[32:33] offset:256
	s_or_b64 exec, exec, s[4:5]
	s_mov_b64 s[4:5], 0
